# P1 in-projection: column-tile permutation (16<->1, 20<->5, 13<->3, 17<->7) so the 4-unit workgroups carry no rope-epilogue tiles
# baseline (speedup 1.0000x reference)
.LBB0_116:
	s_load_dwordx16 s[4:19], s[0:1], 0x40
	s_cmp_lt_i32 s68, 2
	s_cselect_b64 s[0:1], -1, 0
	s_cmp_gt_i32 s69, 1
	s_waitcnt lgkmcnt(0)
	v_writelane_b32 v254, s4, 21
	s_nop 1
	v_writelane_b32 v254, s5, 22
	v_writelane_b32 v254, s6, 23
	v_writelane_b32 v254, s7, 24
	v_writelane_b32 v254, s8, 25
	v_writelane_b32 v254, s9, 26
	v_writelane_b32 v254, s10, 27
	v_writelane_b32 v254, s11, 28
	v_writelane_b32 v254, s12, 29
	v_writelane_b32 v254, s13, 30
	v_writelane_b32 v254, s14, 31
	v_writelane_b32 v254, s15, 32
	v_writelane_b32 v254, s16, 33
	v_writelane_b32 v254, s17, 34
	v_writelane_b32 v254, s18, 35
	v_writelane_b32 v254, s19, 36
	s_cselect_b64 s[4:5], -1, 0
	s_and_b64 s[0:1], s[0:1], s[4:5]
	s_mov_b64 s[4:5], s[40:41]
	s_mov_b64 s[6:7], s[42:43]
	s_mov_b64 s[8:9], s[44:45]
	s_mov_b64 s[10:11], s[46:47]
	s_mov_b64 s[14:15], s[50:51]
	v_writelane_b32 v254, s4, 37
	s_andn2_b64 vcc, exec, s[0:1]
	s_nop 0
	v_writelane_b32 v254, s5, 38
	v_writelane_b32 v254, s6, 39
	v_writelane_b32 v254, s7, 40
	v_writelane_b32 v254, s8, 41
	v_writelane_b32 v254, s9, 42
	v_writelane_b32 v254, s10, 43
	v_writelane_b32 v254, s11, 44
	v_writelane_b32 v254, s12, 45
	v_writelane_b32 v254, s13, 46
	v_writelane_b32 v254, s14, 47
	v_writelane_b32 v254, s15, 48
	v_writelane_b32 v254, s16, 49
	v_writelane_b32 v254, s17, 50
	v_writelane_b32 v254, s18, 51
	v_writelane_b32 v254, s19, 52
	s_cbranch_vccnz .LBB0_259
	v_lshrrev_b32_e32 v4, 5, v0
	v_lshrrev_b32_e32 v6, 1, v0
	v_lshlrev_b32_e32 v2, 4, v0
	v_and_b32_e32 v1, 32, v0
	v_and_b32_e32 v4, 4, v4
	v_bfe_u32 v5, v0, 2, 2
	v_and_b32_e32 v142, 24, v6
	v_bfe_u32 v175, v0, 2, 4
	v_bitop3_b32 v1, v2, v1, 48 bitop3:0x6c
	v_and_b32_e32 v174, 64, v0
	v_or3_b32 v4, v4, v5, v142
	v_lshrrev_b32_e32 v5, 3, v0
	v_or_b32_e32 v176, 0x2000, v2
	v_or_b32_e32 v3, v1, v174
	v_and_or_b32 v6, v5, 48, v175
	v_and_or_b32 v5, v5, 32, v4
	v_lshrrev_b32_e32 v2, 7, v176
	s_movk_i32 s0, 0x70
	v_lshl_or_b32 v136, v5, 12, v3
	v_and_or_b32 v5, v2, s0, v175
	s_movk_i32 s0, 0x60
	v_and_or_b32 v2, v2, s0, v4
	v_lshl_or_b32 v134, v6, 12, v3
	v_lshl_or_b32 v138, v5, 12, v3
	v_lshl_or_b32 v140, v2, 12, v3
	v_lshlrev_b32_e32 v2, 6, v0
	v_lshlrev_b32_e32 v3, 2, v0
	v_lshlrev_b32_e32 v177, 1, v142
	v_and_b32_e32 v2, 0x3c0, v2
	v_and_b32_e32 v3, 32, v3
	v_mov_b32_e32 v143, v0
	v_readfirstlane_b32 s5, v0
	v_and_b32_e32 v147, 15, v0
	s_cmpk_gt_i32 s2, 0x31f
	v_bitop3_b32 v178, v177, v3, v2 bitop3:0x36
	s_cbranch_scc1 .LBB0_137
	s_add_u32 s3, s94, 0x43000000
	s_addc_u32 s12, s95, 0
	s_add_u32 s13, s94, 0x400000
	s_addc_u32 s14, s95, 0
	s_ashr_i32 s16, s2, 31
	s_lshr_b32 s0, s16, 29
	s_add_i32 s0, s2, s0
	s_lshr_b32 s6, s5, 6
	s_ashr_i32 s1, s0, 3
	s_and_b32 s0, s0, -8
	s_lshr_b32 s8, s5, 8
	s_lshl_b32 s15, s6, 10
	s_sub_i32 s0, s2, s0
	s_cmp_lt_i32 s0, 0
	s_movk_i32 s17, 0x65
	s_cselect_b32 s4, s17, 0x64
	s_mul_i32 s0, s0, s4
	s_add_i32 s0, s0, s1
	s_mul_hi_i32 s1, s0, 0x51eb851f
	s_lshr_b32 s4, s1, 31
	s_ashr_i32 s1, s1, 6
	s_add_i32 s1, s1, s4
	s_lshl_b32 s7, s1, 3
	s_mulk_i32 s1, 0xc8
	s_sub_i32 s0, s0, s1
	s_sext_i32_i16 s1, s0
	s_bfe_u32 s1, s1, 0x3001c
	s_add_i32 s1, s0, s1
	s_sext_i32_i16 s4, s1
	s_and_b32 s1, s1, 0xfff8
	s_sub_i32 s0, s0, s1
	s_sext_i32_i16 s0, s0
	s_lshr_b32 s4, s4, 3
	s_lshl_b32 s98, 1, s4
	s_and_b32 s99, s98, 0x110022
	s_cselect_b32 s99, 17, 0
	s_xor_b32 s4, s4, s99
	s_and_b32 s99, s98, 0x2008
	s_cselect_b32 s99, 14, 0
	s_xor_b32 s4, s4, s99
	s_and_b32 s99, s98, 0x20080
	s_cselect_b32 s99, 22, 0
	s_xor_b32 s4, s4, s99
	s_add_i32 s28, s7, s0
	s_ashr_i32 s29, s28, 31
	s_bfe_i64 s[10:11], s[4:5], 0x100000
	s_lshl_b64 s[0:1], s[28:29], 20
	s_lshl_b64 s[10:11], s[10:11], 20
	s_add_u32 s34, s13, s10
	s_addc_u32 s35, s14, s11
	s_add_i32 s18, s15, 0
	s_add_i32 m0, s18, 0x10000
	v_mov_b32_e32 v145, 0
	global_load_lds_dwordx4 v136, s[34:35]
	s_add_i32 m0, s18, 0x12000
	s_add_u32 s10, s34, 0x80000
	global_load_lds_dwordx4 v140, s[34:35]
	s_addc_u32 s11, s35, 0
	s_add_i32 m0, s18, 0x14000
	v_mov_b32_e32 v137, v145
	global_load_lds_dwordx4 v136, s[10:11]
	s_add_i32 m0, s18, 0x16000
	s_add_u32 s30, s3, s0
	s_addc_u32 s31, s12, s1
	s_add_i32 s19, s18, 0x2000
	global_load_lds_dwordx4 v140, s[10:11]
	s_mov_b32 m0, s18
	s_add_u32 s0, s30, 0x80000
	global_load_lds_dwordx4 v134, s[30:31]
	s_mov_b32 m0, s19
	s_addc_u32 s1, s31, 0
	s_add_i32 s22, s18, 0x4000
	global_load_lds_dwordx4 v138, s[30:31]
	s_mov_b32 m0, s22
	s_add_i32 s23, s18, 0x6000
	global_load_lds_dwordx4 v134, s[0:1]
	s_mov_b32 m0, s23
	v_mov_b32_e32 v141, v145
	global_load_lds_dwordx4 v138, s[0:1]
	v_mov_b32_e32 v135, v145
	v_mov_b32_e32 v139, v145
	s_cmp_eq_u32 s8, 1
	s_mov_b32 s38, 0
	v_lshl_add_u64 v[8:9], s[34:35], 0, v[136:137]
	v_lshl_add_u64 v[6:7], s[34:35], 0, v[140:141]
	v_lshl_add_u64 v[2:3], s[30:31], 0, v[134:135]
	s_cselect_b64 s[0:1], -1, 0
	s_cmp_lg_u32 s8, 1
	v_lshl_add_u64 v[4:5], s[30:31], 0, v[138:139]
	s_cbranch_scc1 .LBB0_120
	s_barrier

.LBB0_123:
	s_add_i32 s38, s38, 1
	s_mul_i32 s4, s38, s41
	s_mul_hi_u32 s5, s38, s33
	s_add_i32 s5, s5, s4
	s_mul_i32 s4, s38, s33
	s_add_u32 s24, s4, s2
	s_addc_u32 s25, s5, s16
	v_cmp_gt_i64_e32 vcc, s[24:25], v[156:157]
	v_cmp_lt_i64_e64 s[4:5], s[24:25], v[154:155]
	s_cbranch_vccnz .LBB0_125
	s_ashr_i32 s10, s24, 31
	s_lshr_b32 s10, s10, 29
	s_add_i32 s10, s24, s10
	s_ashr_i32 s11, s10, 3
	s_and_b32 s10, s10, -8
	s_sub_i32 s10, s24, s10
	s_cmp_lt_i32 s10, 0
	s_cselect_b32 s20, s17, 0x64
	s_mul_i32 s10, s10, s20
	s_add_i32 s10, s10, s11
	s_mul_hi_i32 s11, s10, 0x51eb851f
	s_lshr_b32 s20, s11, 31
	s_ashr_i32 s11, s11, 6
	s_add_i32 s11, s11, s20
	s_lshl_b32 s20, s11, 3
	s_sub_i32 s21, 32, s20
	s_min_i32 s21, s21, 8
	s_abs_i32 s24, s21
	v_cvt_f32_u32_e32 v2, s24
	s_sub_i32 s26, 0, s24
	s_mulk_i32 s11, 0xc8
	s_sub_i32 s11, s10, s11
	v_rcp_iflag_f32_e32 v2, v2
	s_abs_i32 s10, s11
	s_xor_b32 s25, s11, s21
	s_ashr_i32 s25, s25, 31
	v_mul_f32_e32 v2, 0x4f7ffffe, v2
	v_cvt_u32_f32_e32 v2, v2
	s_nop 0
	v_readfirstlane_b32 s27, v2
	s_mul_i32 s26, s26, s27
	s_mul_hi_u32 s26, s27, s26
	s_add_i32 s27, s27, s26
	s_mul_hi_u32 s26, s10, s27
	s_mul_i32 s27, s26, s24
	s_sub_i32 s10, s10, s27
	s_add_i32 s29, s26, 1
	s_sub_i32 s27, s10, s24
	s_cmp_ge_u32 s10, s24
	s_cselect_b32 s26, s29, s26
	s_cselect_b32 s10, s27, s10
	s_add_i32 s27, s26, 1
	s_cmp_ge_u32 s10, s24
	s_cselect_b32 s10, s27, s26
	s_xor_b32 s10, s10, s25
	s_sub_i32 s10, s10, s25
	s_mul_i32 s21, s10, s21
	s_lshl_b32 s98, 1, s10
	s_and_b32 s99, s98, 0x110022
	s_cselect_b32 s99, 17, 0
	s_xor_b32 s10, s10, s99
	s_and_b32 s99, s98, 0x2008
	s_cselect_b32 s99, 14, 0
	s_xor_b32 s10, s10, s99
	s_and_b32 s99, s98, 0x20080
	s_cselect_b32 s99, 22, 0
	s_xor_b32 s10, s10, s99
	s_sub_i32 s11, s11, s21
	s_add_i32 s20, s20, s11
